# baseline (speedup 1.0000x reference)
_Z11attn_kernelPKfS0_S0_PKcS2_PKDv4_jS0_S0_S0_S0_Pf:
	s_load_dwordx8 s[4:11], s[0:1], 0x0
	s_load_dwordx8 s[12:19], s[0:1], 0x20
	v_readfirstlane_b32 s20, v0
	s_bfe_u32 s28, s2, 0x10002
	s_lshr_b32 s29, s20, 6
	s_lshr_b32 s3, s20, 8
	s_bfe_u32 s30, s20, 0x20006
	s_lshr_b32 s31, s2, 3
	s_lshl_b32 s24, s28, 18
	s_waitcnt lgkmcnt(0)
	s_add_u32 s20, s10, s24
	s_addc_u32 s10, s11, 0
	s_and_b32 s21, s10, 0xffff
	s_add_u32 s24, s12, s24
	s_addc_u32 s10, s13, 0
	v_and_b32_e32 v1, 63, v0
	s_and_b32 s25, s10, 0xffff
	s_lshl_b32 s10, s30, 10
	s_lshl_b32 s38, s3, 12
	v_lshlrev_b32_e32 v2, 4, v1
	s_or_b32 s35, s10, s38
	v_lshl_or_b32 v2, s3, 17, v2
	s_cmp_lg_u32 0, -1
	v_or_b32_e32 v174, s10, v2
	s_cselect_b32 s10, 0, 0
	s_mov_b32 s36, 0
	s_mov_b32 s23, 0x20000
	s_mov_b32 s22, 0x40000
	s_add_i32 s33, s35, s10
	s_mov_b32 m0, s33
	s_nop 0
	buffer_load_dwordx4 v174, s[20:23], s36 offen lds
	s_mov_b32 s26, s22
	s_mov_b32 s27, s23
	s_add_i32 s34, s33, 0xc000
	s_mov_b32 m0, s34
	s_nop 0
	buffer_load_dwordx4 v174, s[24:27], s36 offen lds
	s_add_i32 s10, s33, 0x4000
	s_movk_i32 s37, 0x1000
	s_mov_b32 m0, s10
	s_nop 0
	buffer_load_dwordx4 v174, s[20:23], s37 offen lds
	s_add_i32 s10, s33, 0x8000
	s_movk_i32 s11, 0x2000
	s_mov_b32 m0, s10
	s_nop 0
	buffer_load_dwordx4 v174, s[20:23], s11 offen lds
	s_lshl_b32 s10, s2, 7
	s_and_b32 s10, s10, 0x380
	s_lshl_b32 s11, s31, 2
	s_add_i32 s10, s10, s11
	s_or_b32 s10, s30, s10
	v_and_b32_e32 v172, 31, v0
	v_lshl_or_b32 v140, s10, 7, v1
	v_mov_b32_e32 v141, 0
	v_lshl_add_u64 v[6:7], v[140:141], 4, s[14:15]
	v_ashrrev_i32_e32 v9, 31, v140
	v_mov_b32_e32 v8, v140
	v_lshl_or_b32 v140, s10, 5, v172
	v_lshlrev_b64 v[4:5], 2, v[140:141]
	v_lshl_add_u64 v[2:3], s[16:17], 0, v[4:5]
	global_load_dword v2, v[2:3], off
	v_lshl_add_u64 v[8:9], v[8:9], 4, s[14:15]
	global_load_dwordx4 v[116:119], v[6:7], off
	global_load_dwordx4 v[120:123], v[8:9], off offset:1024
	s_load_dwordx4 s[12:15], s[0:1], 0x40
	s_load_dwordx2 s[10:11], s[0:1], 0x50
	v_lshlrev_b32_e32 v173, 2, v1
	v_lshl_or_b32 v3, s28, 11, v173
	s_waitcnt lgkmcnt(0)
	global_load_dword v44, v3, s[14:15] offset:256
	global_load_dword v45, v3, s[14:15]
	v_bfe_u32 v175, v0, 5, 1
	v_lshlrev_b32_e32 v0, 11, v175
	v_lshlrev_b32_e32 v3, 4, v172
	s_add_i32 s0, s38, 0
	v_lshl_add_u64 v[4:5], s[12:13], 0, v[4:5]
	v_add3_u32 v176, s0, v0, v3
	global_load_dword v0, v[4:5], off
	v_lshrrev_b32_e32 v124, 2, v1
	v_lshrrev_b32_e32 v125, 4, v1
	v_xor_b32_e32 v124, v124, v125
	v_and_b32_e32 v124, 1, v124
	v_add_u32_e32 v124, -1, v124
	v_and_b32_e32 v124, 0x38383838, v124
	v_mov_b32_e32 v200, 0
	v_mov_b32_e32 v201, 0
	v_mov_b32_e32 v202, 0
	v_mov_b32_e32 v203, 0
	v_mov_b32_e32 v204, 0
	v_mov_b32_e32 v125, v124
	v_mov_b32_e32 v126, v124
	v_mov_b32_e32 v127, v124
	v_mov_b32_e32 v128, v124
	v_mov_b32_e32 v129, v124
	v_mov_b32_e32 v130, v124
	v_mov_b32_e32 v131, v124
	v_mov_b32_e32 v140, 0x7f7f7f7f
	s_mov_b32 s0, 0xf800000
	s_movk_i32 s15, 0x3000
	s_mov_b32 s12, 1
	s_movk_i32 s14, 0x4000
	s_mov_b32 s13, 0x8000
	v_mov_b64_e32 v[132:133], 0
	v_mov_b64_e32 v[134:135], 0
	v_mov_b64_e32 v[136:137], 0
	v_mov_b64_e32 v[138:139], 0
	s_waitcnt vmcnt(5)
	v_mov_b32_e32 v4, v2
	v_mov_b32_e32 v5, v2
	v_mov_b32_e32 v6, v2
	v_mov_b32_e32 v7, v2
	v_mov_b32_e32 v8, v2
	v_mov_b32_e32 v9, v2
	v_mov_b32_e32 v10, v2
	v_mov_b32_e32 v11, v2
	v_mov_b32_e32 v12, v2
	v_mov_b32_e32 v13, v2
	v_mov_b32_e32 v14, v2
	v_mov_b32_e32 v15, v2
	v_mov_b32_e32 v16, v2
	v_mov_b32_e32 v17, v2
	v_mov_b32_e32 v3, v2
	v_mov_b64_e32 v[18:19], v[16:17]
	v_mov_b64_e32 v[16:17], v[14:15]
	v_mov_b64_e32 v[14:15], v[12:13]
	v_mov_b64_e32 v[12:13], v[10:11]
	v_mov_b64_e32 v[10:11], v[8:9]
	v_mov_b64_e32 v[8:9], v[6:7]
	v_mov_b64_e32 v[6:7], v[4:5]
	v_mov_b64_e32 v[4:5], v[2:3]
	s_waitcnt vmcnt(0) lgkmcnt(0)
	s_barrier
	ds_read_b128 v[24:27], v176 offset:1024
	ds_read_b128 v[20:23], v176
	ds_read_b128 v[36:39], v176 offset:512
	ds_read_b128 v[40:43], v176 offset:1536
	ds_read_b128 v[84:87], v176 offset:16384
	ds_read_b128 v[92:95], v176 offset:16896
	ds_read_b128 v[88:91], v176 offset:17408
	ds_read_b128 v[96:99], v176 offset:17920
	s_waitcnt vmcnt(3) lgkmcnt(6)
	v_mfma_f32_32x32x64_f8f6f4 v[20:35], v[20:27], v[116:123], v[4:19]
	s_waitcnt vmcnt(2)
	v_max_f32_e32 v3, v44, v44
	s_waitcnt vmcnt(1)
	v_max_f32_e32 v44, v45, v45
	v_max_f32_e32 v44, v44, v3
	s_nop 1
	v_max_f32_dpp v44, v44, v44 quad_perm:[1,0,3,2] row_mask:0xf bank_mask:0xf
	s_nop 1
	v_max_f32_dpp v44, v44, v44 quad_perm:[2,3,0,1] row_mask:0xf bank_mask:0xf
	s_nop 1
	v_max_f32_dpp v44, v44, v44 row_half_mirror row_mask:0xf bank_mask:0xf
	s_nop 1
	v_max_f32_dpp v44, v44, v44 row_mirror row_mask:0xf bank_mask:0xf
	s_nop 1
	v_max_f32_dpp v44, v44, v44 row_bcast:15 row_mask:0xa bank_mask:0xf
	s_nop 1
	v_max_f32_dpp v44, v44, v44 row_bcast:31 row_mask:0xc bank_mask:0xf
	s_nop 1
	v_readlane_b32 s47, v44, 63
	s_waitcnt vmcnt(0) lgkmcnt(0)
	s_barrier
	v_mfma_f32_32x32x64_f8f6f4 v[4:19], v[36:43], v[116:123], v[4:19]
	s_mov_b32 m0, s33
	s_nop 0
	buffer_load_dwordx4 v174, s[20:23], s15 offen lds
	s_add_i32 s15, s34, 0x4000
	s_mov_b32 m0, s15
	s_nop 0
	buffer_load_dwordx4 v174, s[24:27], s37 offen lds
	s_nop 1
	v_max_f32_e32 v3, v21, v21
	v_max_f32_e32 v36, v20, v20
	v_max_f32_e32 v3, v36, v3
	s_nop 7
	v_max3_f32 v37, v22, v23, v5
	v_max3_f32 v36, v37, v26, v27
	v_max3_f32 v3, v3, v4, v6
	v_max3_f32 v3, v3, v7, v24
	v_max3_f32 v36, v36, v10, v11
	v_max3_f32 v3, v3, v25, v8
	v_max3_f32 v36, v36, v30, v31
	v_max3_f32 v3, v3, v9, v28
	v_max3_f32 v36, v36, v14, v15
	v_max3_f32 v3, v3, v29, v12
	v_max3_f32 v36, v36, v34, v35
	v_max3_f32 v3, v3, v13, v32
	v_max3_f32 v36, v36, v18, v19
	v_max3_f32 v3, v3, v33, v16
	v_max3_f32 v3, v3, v17, v36
	v_mov_b32_e32 v36, v3
	s_nop 1
	v_permlane32_swap_b32_e32 v3, v36
	v_max_f32_e32 v36, v36, v36
	v_max_f32_e32 v3, v3, v3
	v_max_f32_e32 v3, v3, v36
	v_sub_f32_e32 v36, 0xc0400000, v3
	v_add_f32_e32 v20, v36, v20
	v_add_f32_e32 v21, v36, v21
	v_add_f32_e32 v22, v36, v22
	v_add_f32_e32 v23, v36, v23
	v_add_f32_e32 v24, v36, v24
	v_add_f32_e32 v25, v36, v25
	v_add_f32_e32 v26, v36, v26
	v_add_f32_e32 v27, v36, v27
	v_add_f32_e32 v28, v36, v28
	v_add_f32_e32 v29, v36, v29
	v_mov_b32_e32 v37, s47
	v_mul_f32_e32 v38, 0x4f800000, v37
	v_cmp_gt_f32_e32 vcc, s0, v37
	v_add_f32_e32 v30, v36, v30
	v_add_f32_e32 v31, v36, v31
	v_cndmask_b32_e32 v37, v37, v38, vcc
	v_sqrt_f32_e32 v38, v37
	v_add_f32_e32 v32, v36, v32
	v_add_f32_e32 v33, v36, v33
	v_add_f32_e32 v34, v36, v34
	v_add_f32_e32 v35, v36, v35
	v_add_f32_e32 v4, v36, v4
	v_add_f32_e32 v5, v36, v5
	v_add_f32_e32 v6, v36, v6
	v_add_f32_e32 v7, v36, v7
	v_add_f32_e32 v8, v36, v8
	v_add_f32_e32 v9, v36, v9
	v_add_f32_e32 v10, v36, v10
	v_add_f32_e32 v11, v36, v11
	v_add_f32_e32 v12, v36, v12
	v_add_f32_e32 v13, v36, v13
	v_add_f32_e32 v14, v36, v14
	v_add_f32_e32 v15, v36, v15
	v_add_f32_e32 v16, v36, v16
	v_add_f32_e32 v17, v36, v17
	v_add_f32_e32 v18, v36, v18
	v_add_f32_e32 v19, v36, v19
	v_add_u32_e32 v36, -1, v38
	v_fma_f32 v39, -v36, v38, v37
	v_cmp_ge_f32_e64 s[0:1], 0, v39
	v_add_u32_e32 v39, 1, v38
	v_exp_f32_e32 v161, v20
	v_cndmask_b32_e64 v36, v38, v36, s[0:1]
	v_fma_f32 v38, -v39, v38, v37
	v_cmp_lt_f32_e64 s[0:1], 0, v38
	v_exp_f32_e32 v100, v4
	v_exp_f32_e32 v163, v21
	v_cndmask_b32_e64 v36, v36, v39, s[0:1]
	v_mul_f32_e32 v38, 0x37800000, v36
	v_cndmask_b32_e32 v36, v36, v38, vcc
	v_mov_b32_e32 v38, 0x260
	v_cmp_class_f32_e32 vcc, v37, v38
	s_mov_b32 s0, 0x42700000
	v_exp_f32_e32 v148, v5
	v_cndmask_b32_e32 v36, v36, v37, vcc
	s_waitcnt vmcnt(0)
	v_mul_f32_e32 v0, v36, v0
	v_mul_f32_e32 v0, 0x3f91eb85, v0
	v_exp_f32_e32 v162, v22
	v_exp_f32_e32 v101, v6
	v_exp_f32_e32 v164, v23
	v_exp_f32_e32 v102, v7
	v_exp_f32_e32 v150, v24
	v_exp_f32_e32 v143, v8
	v_exp_f32_e32 v154, v25
	v_exp_f32_e32 v146, v9
	v_exp_f32_e32 v152, v26
	v_exp_f32_e32 v145, v10
	v_exp_f32_e32 v157, v27
	v_exp_f32_e32 v147, v11
	v_exp_f32_e32 v149, v28
	v_exp_f32_e32 v69, v12
	v_exp_f32_e32 v153, v29
	v_exp_f32_e32 v109, v13
	v_exp_f32_e32 v151, v30
	v_exp_f32_e32 v108, v14
	v_exp_f32_e32 v156, v31
	v_exp_f32_e32 v142, v15
	v_exp_f32_e32 v155, v32
	v_exp_f32_e32 v110, v16
	v_exp_f32_e32 v159, v33
	v_exp_f32_e32 v144, v17
	v_exp_f32_e32 v158, v34
	v_exp_f32_e32 v111, v18
	v_exp_f32_e32 v160, v35
	v_exp_f32_e32 v114, v19
	v_cmp_nge_f32_e64 s[0:1], s0, v0
	v_sub_f32_e32 v0, v2, v3
	v_add_f32_e32 v36, 0xc0400000, v0
	v_mov_b32_e32 v37, v36
	v_mov_b64_e32 v[38:39], v[36:37]
	v_mov_b64_e32 v[40:41], v[36:37]
	v_mov_b64_e32 v[42:43], v[36:37]
	v_mov_b64_e32 v[44:45], v[36:37]
	v_mov_b64_e32 v[46:47], v[36:37]
	v_mov_b64_e32 v[48:49], v[36:37]
	v_mov_b64_e32 v[50:51], v[36:37]
	v_mov_b64_e32 v[4:5], 0
	v_mov_b64_e32 v[6:7], 0
	v_mov_b64_e32 v[8:9], 0
	v_mov_b64_e32 v[10:11], 0
	v_mov_b64_e32 v[12:13], 0
	v_mov_b64_e32 v[14:15], 0
	v_mov_b64_e32 v[16:17], 0
	v_mov_b64_e32 v[18:19], 0
	v_mov_b64_e32 v[20:21], 0
	v_mov_b64_e32 v[22:23], 0
	v_mov_b64_e32 v[24:25], 0
	v_mov_b64_e32 v[26:27], 0
	v_mov_b64_e32 v[28:29], 0
	v_mov_b64_e32 v[30:31], 0
	v_mov_b64_e32 v[32:33], 0
	v_mov_b64_e32 v[34:35], 0
	v_mov_b32_e32 v0, v141
